# spatial: one static s_setprio 1 for the second-arriving workgroup of each CU pair (wg id >= 256)
# speedup vs baseline: 1.0010x; 1.0010x over previous
_Z9k_spatialPKDF16_S0_S0_PfPDF16_:
	s_load_dwordx4 s[4:7], s[0:1], 0x0
	s_load_dwordx2 s[10:11], s[0:1], 0x10
	s_cmp_lt_u32 s2, 0x100
	s_cbranch_scc1 .Lsp_noprio
	s_setprio 1
.Lsp_noprio:
	s_mul_hi_i32 s9, s2, 0x3140
	s_mul_i32 s8, s2, 0x3140
	s_lshl_b64 s[8:9], s[8:9], 1
	v_and_b32_e32 v2, 7, v0
	v_lshrrev_b32_e32 v3, 3, v0
	v_lshlrev_b32_e32 v10, 4, v2
	v_lshl_or_b32 v4, v3, 7, v10
	v_add_u32_e32 v5, 0x1c00, v4
	v_add_u32_e32 v6, 0x3800, v4
	v_add_u32_e32 v7, 0x5400, v4
	v_lshrrev_b32_e32 v8, 1, v0
	v_and_b32_e32 v108, 31, v0
	v_and_b32_e32 v115, 0xe0, v8
	v_or_b32_e32 v109, v115, v108
	s_movk_i32 s3, 0xc5
	v_mov_b32_e32 v8, 0xc4
	v_cmp_gt_u32_e64 s[12:13], s3, v109
	v_bfe_u32 v1, v0, 5, 1
	v_lshlrev_b32_e32 v111, 4, v1
	s_nop 1
	v_cndmask_b32_e64 v110, v8, v109, s[12:13]
	v_lshl_or_b32 v9, v110, 7, v111
	s_movk_i32 s3, 0xe8
	v_cmp_gt_u32_e32 vcc, s3, v0
	v_or_b32_e32 v14, 0x6200, v10
	s_nop 1
	v_cndmask_b32_e32 v7, v14, v7, vcc
	s_waitcnt lgkmcnt(0)
	s_add_u32 s6, s6, s8
	s_addc_u32 s7, s7, s9
	s_add_u32 s10, s10, s8
	s_addc_u32 s11, s11, s9
	s_add_u32 s4, s4, s8
	s_addc_u32 s5, s5, s9
	global_load_dwordx4 v[18:21], v4, s[6:7] nt
	global_load_dwordx4 v[22:25], v4, s[10:11] nt
	global_load_dwordx4 v[26:29], v5, s[6:7] nt
	global_load_dwordx4 v[30:33], v5, s[10:11] nt
	global_load_dwordx4 v[34:37], v6, s[6:7] nt
	global_load_dwordx4 v[38:41], v6, s[10:11] nt
	global_load_dwordx4 v[42:45], v7, s[6:7] nt
	global_load_dwordx4 v[46:49], v7, s[10:11] nt
	global_load_dwordx4 v[74:77], v9, s[4:5] offset:0 nt
	global_load_dwordx4 v[78:81], v9, s[4:5] offset:32 nt
	global_load_dwordx4 v[82:85], v9, s[4:5] offset:64 nt
	global_load_dwordx4 v[86:89], v9, s[4:5] offset:96 nt
	s_movk_i32 s3, 0x90
	v_lshlrev_b32_e32 v11, 3, v2
	v_mul_u32_u24_e32 v16, 0x1c8, v11
	v_mad_u32_u24 v12, v3, s3, v10
	v_lshl_add_u32 v13, v3, 1, v16
	v_mad_u32_u24 v112, v108, s3, v111
	s_waitcnt vmcnt(11)
	ds_write_b128 v12, v[18:21] offset:0
	s_waitcnt vmcnt(10)
	ds_write_b16 v13, v22 offset:32256
	ds_write_b16_d16_hi v13, v22 offset:32712
	ds_write_b16 v13, v23 offset:33168
	ds_write_b16_d16_hi v13, v23 offset:33624
	ds_write_b16 v13, v24 offset:34080
	ds_write_b16_d16_hi v13, v24 offset:34536
	ds_write_b16 v13, v25 offset:34992
	ds_write_b16_d16_hi v13, v25 offset:35448
	s_waitcnt vmcnt(9)
	ds_write_b128 v12, v[26:29] offset:8064
	s_waitcnt vmcnt(8)
	ds_write_b16 v13, v30 offset:32368
	ds_write_b16_d16_hi v13, v30 offset:32824
	ds_write_b16 v13, v31 offset:33280
	ds_write_b16_d16_hi v13, v31 offset:33736
	ds_write_b16 v13, v32 offset:34192
	ds_write_b16_d16_hi v13, v32 offset:34648
	ds_write_b16 v13, v33 offset:35104
	ds_write_b16_d16_hi v13, v33 offset:35560
	s_waitcnt vmcnt(7)
	ds_write_b128 v12, v[34:37] offset:16128
	s_waitcnt vmcnt(6)
	ds_write_b16 v13, v38 offset:32480
	ds_write_b16_d16_hi v13, v38 offset:32936
	ds_write_b16 v13, v39 offset:33392
	ds_write_b16_d16_hi v13, v39 offset:33848
	ds_write_b16 v13, v40 offset:34304
	ds_write_b16_d16_hi v13, v40 offset:34760
	ds_write_b16 v13, v41 offset:35216
	ds_write_b16_d16_hi v13, v41 offset:35672
	s_waitcnt vmcnt(5)
	v_cndmask_b32_e32 v42, 0, v42, vcc
	v_cndmask_b32_e32 v43, 0, v43, vcc
	v_cndmask_b32_e32 v44, 0, v44, vcc
	v_cndmask_b32_e32 v45, 0, v45, vcc
	ds_write_b128 v12, v[42:45] offset:24192
	s_waitcnt vmcnt(4)
	v_cndmask_b32_e32 v46, 0, v46, vcc
	v_cndmask_b32_e32 v47, 0, v47, vcc
	v_cndmask_b32_e32 v48, 0, v48, vcc
	v_cndmask_b32_e32 v49, 0, v49, vcc
	ds_write_b16 v13, v46 offset:32592
	ds_write_b16_d16_hi v13, v46 offset:33048
	ds_write_b16 v13, v47 offset:33504
	ds_write_b16_d16_hi v13, v47 offset:33960
	ds_write_b16 v13, v48 offset:34416
	ds_write_b16_d16_hi v13, v48 offset:34872
	ds_write_b16 v13, v49 offset:35328
	ds_write_b16_d16_hi v13, v49 offset:35784
	s_load_dwordx2 s[8:9], s[0:1], 0x20
	s_load_dwordx2 s[10:11], s[0:1], 0x18
	s_mov_b32 s16, 0x3e38aa3b
	s_mov_b32 s17, 0xf149f2ca
	v_cmp_eq_u32_e64 s[14:15], 0, v1
	v_mul_u32_u24_e32 v113, 0x1c8, v108
	v_lshl_add_u32 v113, v1, 3, v113
	v_add_u32_e32 v113, 0x7e00, v113
	v_add_u32_e32 v114, 0x3900, v113
	v_mov_b32_e32 v106, s17
	s_waitcnt vmcnt(0) lgkmcnt(0)
	s_barrier
	ds_read_b128 v[66:69], v112 offset:0
	ds_read_b128 v[70:73], v112 offset:32
	s_waitcnt lgkmcnt(1)
	v_mfma_f32_32x32x16_f16 v[2:17], v[66:69], v[74:77], 0
	ds_read_b128 v[66:69], v112 offset:64
	s_waitcnt lgkmcnt(1)
	v_mfma_f32_32x32x16_f16 v[2:17], v[70:73], v[78:81], v[2:17]
	ds_read_b128 v[70:73], v112 offset:96
	s_waitcnt lgkmcnt(1)
	v_mfma_f32_32x32x16_f16 v[2:17], v[66:69], v[82:85], v[2:17]
	s_waitcnt lgkmcnt(0)
	v_mfma_f32_32x32x16_f16 v[2:17], v[70:73], v[86:89], v[2:17]
	ds_read_b128 v[66:69], v112 offset:4608
	ds_read_b128 v[70:73], v112 offset:4640
	s_waitcnt lgkmcnt(1)
	v_mfma_f32_32x32x16_f16 v[50:65], v[66:69], v[74:77], 0
	ds_read_b128 v[66:69], v112 offset:4672
	s_waitcnt lgkmcnt(1)
	v_mfma_f32_32x32x16_f16 v[50:65], v[70:73], v[78:81], v[50:65]
	ds_read_b128 v[70:73], v112 offset:4704
	s_waitcnt lgkmcnt(1)
	v_mfma_f32_32x32x16_f16 v[50:65], v[66:69], v[82:85], v[50:65]
	s_waitcnt lgkmcnt(0)
	v_mfma_f32_32x32x16_f16 v[50:65], v[70:73], v[86:89], v[50:65]
	v_max3_f32 v106, v106, v2, v3
	v_max3_f32 v106, v106, v4, v5
	v_max3_f32 v106, v106, v6, v7
	v_max3_f32 v106, v106, v8, v9
	v_max3_f32 v106, v106, v10, v11
	v_max3_f32 v106, v106, v12, v13
	v_max3_f32 v106, v106, v14, v15
	v_max3_f32 v106, v106, v16, v17
	ds_read_b128 v[66:69], v112 offset:9216
	ds_read_b128 v[70:73], v112 offset:9248
	s_waitcnt lgkmcnt(1)
	v_mfma_f32_32x32x16_f16 v[2:17], v[66:69], v[74:77], 0
	ds_read_b128 v[66:69], v112 offset:9280
	s_waitcnt lgkmcnt(1)
	v_mfma_f32_32x32x16_f16 v[2:17], v[70:73], v[78:81], v[2:17]
	ds_read_b128 v[70:73], v112 offset:9312
	s_waitcnt lgkmcnt(1)
	v_mfma_f32_32x32x16_f16 v[2:17], v[66:69], v[82:85], v[2:17]
	s_waitcnt lgkmcnt(0)
	v_mfma_f32_32x32x16_f16 v[2:17], v[70:73], v[86:89], v[2:17]
	v_max3_f32 v106, v106, v50, v51
	v_max3_f32 v106, v106, v52, v53
	v_max3_f32 v106, v106, v54, v55
	v_max3_f32 v106, v106, v56, v57
	v_max3_f32 v106, v106, v58, v59
	v_max3_f32 v106, v106, v60, v61
	v_max3_f32 v106, v106, v62, v63
	v_max3_f32 v106, v106, v64, v65
	ds_read_b128 v[66:69], v112 offset:13824
	ds_read_b128 v[70:73], v112 offset:13856
	s_waitcnt lgkmcnt(1)
	v_mfma_f32_32x32x16_f16 v[50:65], v[66:69], v[74:77], 0
	ds_read_b128 v[66:69], v112 offset:13888
	s_waitcnt lgkmcnt(1)
	v_mfma_f32_32x32x16_f16 v[50:65], v[70:73], v[78:81], v[50:65]
	ds_read_b128 v[70:73], v112 offset:13920
	s_waitcnt lgkmcnt(1)
	v_mfma_f32_32x32x16_f16 v[50:65], v[66:69], v[82:85], v[50:65]
	s_waitcnt lgkmcnt(0)
	v_mfma_f32_32x32x16_f16 v[50:65], v[70:73], v[86:89], v[50:65]
	v_max3_f32 v106, v106, v2, v3
	v_max3_f32 v106, v106, v4, v5
	v_max3_f32 v106, v106, v6, v7
	v_max3_f32 v106, v106, v8, v9
	v_max3_f32 v106, v106, v10, v11
	v_max3_f32 v106, v106, v12, v13
	v_max3_f32 v106, v106, v14, v15
	v_max3_f32 v106, v106, v16, v17
	ds_read_b128 v[66:69], v112 offset:18432
	ds_read_b128 v[70:73], v112 offset:18464
	s_waitcnt lgkmcnt(1)
	v_mfma_f32_32x32x16_f16 v[18:33], v[66:69], v[74:77], 0
	ds_read_b128 v[66:69], v112 offset:18496
	s_waitcnt lgkmcnt(1)
	v_mfma_f32_32x32x16_f16 v[18:33], v[70:73], v[78:81], v[18:33]
	ds_read_b128 v[70:73], v112 offset:18528
	s_waitcnt lgkmcnt(1)
	v_mfma_f32_32x32x16_f16 v[18:33], v[66:69], v[82:85], v[18:33]
	s_waitcnt lgkmcnt(0)
	v_mfma_f32_32x32x16_f16 v[18:33], v[70:73], v[86:89], v[18:33]
	v_max3_f32 v106, v106, v50, v51
	v_max3_f32 v106, v106, v52, v53
	v_max3_f32 v106, v106, v54, v55
	v_max3_f32 v106, v106, v56, v57
	v_max3_f32 v106, v106, v58, v59
	v_max3_f32 v106, v106, v60, v61
	v_max3_f32 v106, v106, v62, v63
	v_max3_f32 v106, v106, v64, v65
	ds_read_b128 v[66:69], v112 offset:23040
	ds_read_b128 v[70:73], v112 offset:23072
	s_waitcnt lgkmcnt(1)
	v_mfma_f32_32x32x16_f16 v[34:49], v[66:69], v[74:77], 0
	ds_read_b128 v[66:69], v112 offset:23104
	s_waitcnt lgkmcnt(1)
	v_mfma_f32_32x32x16_f16 v[34:49], v[70:73], v[78:81], v[34:49]
	ds_read_b128 v[70:73], v112 offset:23136
	s_waitcnt lgkmcnt(1)
	v_mfma_f32_32x32x16_f16 v[34:49], v[66:69], v[82:85], v[34:49]
	s_waitcnt lgkmcnt(0)
	v_mfma_f32_32x32x16_f16 v[34:49], v[70:73], v[86:89], v[34:49]
	v_max3_f32 v106, v106, v18, v19
	v_max3_f32 v106, v106, v20, v21
	v_max3_f32 v106, v106, v22, v23
	v_max3_f32 v106, v106, v24, v25
	v_max3_f32 v106, v106, v26, v27
	v_max3_f32 v106, v106, v28, v29
	v_max3_f32 v106, v106, v30, v31
	v_max3_f32 v106, v106, v32, v33
	ds_read_b128 v[66:69], v112 offset:27648
	ds_read_b128 v[70:73], v112 offset:27680
	s_waitcnt lgkmcnt(1)
	v_mfma_f32_32x32x16_f16 v[90:105], v[66:69], v[74:77], 0
	ds_read_b128 v[66:69], v112 offset:27712
	s_waitcnt lgkmcnt(1)
	v_mfma_f32_32x32x16_f16 v[90:105], v[70:73], v[78:81], v[90:105]
	ds_read_b128 v[70:73], v112 offset:27744
	s_waitcnt lgkmcnt(1)
	v_mfma_f32_32x32x16_f16 v[90:105], v[66:69], v[82:85], v[90:105]
	s_waitcnt lgkmcnt(0)
	v_mfma_f32_32x32x16_f16 v[90:105], v[70:73], v[86:89], v[90:105]
	v_max3_f32 v106, v106, v34, v35
	v_max3_f32 v106, v106, v36, v37
	v_max3_f32 v106, v106, v38, v39
	v_max3_f32 v106, v106, v40, v41
	v_max3_f32 v106, v106, v42, v43
	v_max3_f32 v106, v106, v44, v45
	v_max3_f32 v106, v106, v46, v47
	v_max3_f32 v106, v106, v48, v49
	s_nop 15
	s_nop 1
	v_mov_b32_e32 v94, s17
	v_mov_b32_e32 v95, s17
	v_mov_b32_e32 v96, s17
	v_mov_b32_e32 v97, s17
	v_mov_b32_e32 v98, s17
	v_mov_b32_e32 v99, s17
	v_mov_b32_e32 v100, s17
	v_mov_b32_e32 v101, s17
	v_mov_b32_e32 v102, s17
	v_mov_b32_e32 v103, s17
	v_mov_b32_e32 v104, s17
	v_mov_b32_e32 v105, s17
	v_mov_b32_e32 v120, s17
	v_cndmask_b32_e64 v91, v120, v91, s[14:15]
	v_cndmask_b32_e64 v92, v120, v92, s[14:15]
	v_cndmask_b32_e64 v93, v120, v93, s[14:15]
	v_max3_f32 v106, v106, v90, v91
	v_max3_f32 v106, v106, v92, v93
	v_max3_f32 v106, v106, v94, v95
	v_max3_f32 v106, v106, v96, v97
	v_max3_f32 v106, v106, v98, v99
	v_max3_f32 v106, v106, v100, v101
	v_max3_f32 v106, v106, v102, v103
	v_max3_f32 v106, v106, v104, v105
	v_mov_b32_e32 v120, v106
	v_mov_b32_e32 v121, v106
	s_nop 1
	v_permlane32_swap_b32_e32 v120, v121
	s_nop 1
	v_max3_f32 v106, v106, v120, v121
	v_mul_f32_e32 v106, s16, v106
	v_mov_b32_e32 v107, 0
	v_fma_f32 v120, v50, s16, -v106
	v_exp_f32_e32 v50, v120
	v_fma_f32 v121, v51, s16, -v106
	v_exp_f32_e32 v51, v121
	v_fma_f32 v122, v52, s16, -v106
	v_exp_f32_e32 v52, v122
	v_fma_f32 v123, v53, s16, -v106
	v_exp_f32_e32 v53, v123
	v_fma_f32 v120, v54, s16, -v106
	v_exp_f32_e32 v54, v120
	v_fma_f32 v121, v55, s16, -v106
	v_exp_f32_e32 v55, v121
	v_fma_f32 v122, v56, s16, -v106
	v_exp_f32_e32 v56, v122
	v_fma_f32 v123, v57, s16, -v106
	v_exp_f32_e32 v57, v123
	v_fma_f32 v120, v58, s16, -v106
	v_exp_f32_e32 v58, v120
	v_fma_f32 v121, v59, s16, -v106
	v_exp_f32_e32 v59, v121
	v_fma_f32 v122, v60, s16, -v106
	v_exp_f32_e32 v60, v122
	v_fma_f32 v123, v61, s16, -v106
	v_exp_f32_e32 v61, v123
	v_fma_f32 v120, v62, s16, -v106
	v_exp_f32_e32 v62, v120
	v_fma_f32 v121, v63, s16, -v106
	v_exp_f32_e32 v63, v121
	v_fma_f32 v122, v64, s16, -v106
	v_exp_f32_e32 v64, v122
	v_fma_f32 v123, v65, s16, -v106
	v_exp_f32_e32 v65, v123
	v_add_f32_e32 v107, v107, v50
	v_add_f32_e32 v107, v107, v51
	v_add_f32_e32 v107, v107, v52
	v_add_f32_e32 v107, v107, v53
	v_add_f32_e32 v107, v107, v54
	v_add_f32_e32 v107, v107, v55
	v_add_f32_e32 v107, v107, v56
	v_add_f32_e32 v107, v107, v57
	v_add_f32_e32 v107, v107, v58
	v_add_f32_e32 v107, v107, v59
	v_add_f32_e32 v107, v107, v60
	v_add_f32_e32 v107, v107, v61
	v_add_f32_e32 v107, v107, v62
	v_add_f32_e32 v107, v107, v63
	v_add_f32_e32 v107, v107, v64
	v_add_f32_e32 v107, v107, v65
	v_cvt_pk_f16_f32 v66, v50, v51
	v_cvt_pk_f16_f32 v67, v52, v53
	v_cvt_pk_f16_f32 v68, v54, v55
	v_cvt_pk_f16_f32 v69, v56, v57
	v_cvt_pk_f16_f32 v70, v58, v59
	v_cvt_pk_f16_f32 v71, v60, v61
	v_cvt_pk_f16_f32 v72, v62, v63
	v_cvt_pk_f16_f32 v73, v64, v65
	v_fma_f32 v120, v18, s16, -v106
	v_exp_f32_e32 v18, v120
	v_fma_f32 v121, v19, s16, -v106
	v_exp_f32_e32 v19, v121
	v_fma_f32 v122, v20, s16, -v106
	v_exp_f32_e32 v20, v122
	v_fma_f32 v123, v21, s16, -v106
	v_exp_f32_e32 v21, v123
	v_fma_f32 v120, v22, s16, -v106
	v_exp_f32_e32 v22, v120
	v_fma_f32 v121, v23, s16, -v106
	v_exp_f32_e32 v23, v121
	v_fma_f32 v122, v24, s16, -v106
	v_exp_f32_e32 v24, v122
	v_fma_f32 v123, v25, s16, -v106
	v_exp_f32_e32 v25, v123
	v_fma_f32 v120, v26, s16, -v106
	v_exp_f32_e32 v26, v120
	v_fma_f32 v121, v27, s16, -v106
	v_exp_f32_e32 v27, v121
	v_fma_f32 v122, v28, s16, -v106
	v_exp_f32_e32 v28, v122
	v_fma_f32 v123, v29, s16, -v106
	v_exp_f32_e32 v29, v123
	v_fma_f32 v120, v30, s16, -v106
	v_exp_f32_e32 v30, v120
	v_fma_f32 v121, v31, s16, -v106
	v_exp_f32_e32 v31, v121
	v_fma_f32 v122, v32, s16, -v106
	v_exp_f32_e32 v32, v122
	v_fma_f32 v123, v33, s16, -v106
	v_exp_f32_e32 v33, v123
	v_add_f32_e32 v107, v107, v18
	v_add_f32_e32 v107, v107, v19
	v_add_f32_e32 v107, v107, v20
	v_add_f32_e32 v107, v107, v21
	v_add_f32_e32 v107, v107, v22
	v_add_f32_e32 v107, v107, v23
	v_add_f32_e32 v107, v107, v24
	v_add_f32_e32 v107, v107, v25
	v_add_f32_e32 v107, v107, v26
	v_add_f32_e32 v107, v107, v27
	v_add_f32_e32 v107, v107, v28
	v_add_f32_e32 v107, v107, v29
	v_add_f32_e32 v107, v107, v30
	v_add_f32_e32 v107, v107, v31
	v_add_f32_e32 v107, v107, v32
	v_add_f32_e32 v107, v107, v33
	v_cvt_pk_f16_f32 v50, v18, v19
	v_cvt_pk_f16_f32 v51, v20, v21
	v_cvt_pk_f16_f32 v52, v22, v23
	v_cvt_pk_f16_f32 v53, v24, v25
	v_cvt_pk_f16_f32 v54, v26, v27
	v_cvt_pk_f16_f32 v55, v28, v29
	v_cvt_pk_f16_f32 v56, v30, v31
	v_cvt_pk_f16_f32 v57, v32, v33
	v_fma_f32 v120, v34, s16, -v106
	v_exp_f32_e32 v34, v120
	v_fma_f32 v121, v35, s16, -v106
	v_exp_f32_e32 v35, v121
	v_fma_f32 v122, v36, s16, -v106
	v_exp_f32_e32 v36, v122
	v_fma_f32 v123, v37, s16, -v106
	v_exp_f32_e32 v37, v123
	v_fma_f32 v120, v38, s16, -v106
	v_exp_f32_e32 v38, v120
	v_fma_f32 v121, v39, s16, -v106
	v_exp_f32_e32 v39, v121
	v_fma_f32 v122, v40, s16, -v106
	v_exp_f32_e32 v40, v122
	v_fma_f32 v123, v41, s16, -v106
	v_exp_f32_e32 v41, v123
	v_fma_f32 v120, v42, s16, -v106
	v_exp_f32_e32 v42, v120
	v_fma_f32 v121, v43, s16, -v106
	v_exp_f32_e32 v43, v121
	v_fma_f32 v122, v44, s16, -v106
	v_exp_f32_e32 v44, v122
	v_fma_f32 v123, v45, s16, -v106
	v_exp_f32_e32 v45, v123
	v_fma_f32 v120, v46, s16, -v106
	v_exp_f32_e32 v46, v120
	v_fma_f32 v121, v47, s16, -v106
	v_exp_f32_e32 v47, v121
	v_fma_f32 v122, v48, s16, -v106
	v_exp_f32_e32 v48, v122
	v_fma_f32 v123, v49, s16, -v106
	v_exp_f32_e32 v49, v123
	v_add_f32_e32 v107, v107, v34
	v_add_f32_e32 v107, v107, v35
	v_add_f32_e32 v107, v107, v36
	v_add_f32_e32 v107, v107, v37
	v_add_f32_e32 v107, v107, v38
	v_add_f32_e32 v107, v107, v39
	v_add_f32_e32 v107, v107, v40
	v_add_f32_e32 v107, v107, v41
	v_add_f32_e32 v107, v107, v42
	v_add_f32_e32 v107, v107, v43
	v_add_f32_e32 v107, v107, v44
	v_add_f32_e32 v107, v107, v45
	v_add_f32_e32 v107, v107, v46
	v_add_f32_e32 v107, v107, v47
	v_add_f32_e32 v107, v107, v48
	v_add_f32_e32 v107, v107, v49
	v_cvt_pk_f16_f32 v116, v34, v35
	v_cvt_pk_f16_f32 v117, v36, v37
	v_cvt_pk_f16_f32 v118, v38, v39
	v_cvt_pk_f16_f32 v119, v40, v41
	v_cvt_pk_f16_f32 v124, v42, v43
	v_cvt_pk_f16_f32 v125, v44, v45
	v_cvt_pk_f16_f32 v126, v46, v47
	v_cvt_pk_f16_f32 v127, v48, v49
	v_mov_b32_e32 v18, 0
	v_mov_b32_e32 v19, 0
	v_mov_b32_e32 v20, 0
	v_mov_b32_e32 v21, 0
	v_mov_b32_e32 v22, 0
	v_mov_b32_e32 v23, 0
	v_mov_b32_e32 v24, 0
	v_mov_b32_e32 v25, 0
	v_mov_b32_e32 v26, 0
	v_mov_b32_e32 v27, 0
	v_mov_b32_e32 v28, 0
	v_mov_b32_e32 v29, 0
	v_mov_b32_e32 v30, 0
	v_mov_b32_e32 v31, 0
	v_mov_b32_e32 v32, 0
	v_mov_b32_e32 v33, 0
	v_mov_b32_e32 v34, 0
	v_mov_b32_e32 v35, 0
	v_mov_b32_e32 v36, 0
	v_mov_b32_e32 v37, 0
	v_mov_b32_e32 v38, 0
	v_mov_b32_e32 v39, 0
	v_mov_b32_e32 v40, 0
	v_mov_b32_e32 v41, 0
	v_mov_b32_e32 v42, 0
	v_mov_b32_e32 v43, 0
	v_mov_b32_e32 v44, 0
	v_mov_b32_e32 v45, 0
	v_mov_b32_e32 v46, 0
	v_mov_b32_e32 v47, 0
	v_mov_b32_e32 v48, 0
	v_mov_b32_e32 v49, 0
	ds_read2_b64 v[58:61], v113 offset0:24 offset1:26
	ds_read2_b64 v[62:65], v114 offset0:24 offset1:26
	s_nop 1
	s_waitcnt lgkmcnt(1)
	v_mfma_f32_32x32x16_f16 v[18:33], v[58:61], v[66:69], v[18:33]
	ds_read2_b64 v[58:61], v113 offset0:28 offset1:30
	s_waitcnt lgkmcnt(1)
	v_mfma_f32_32x32x16_f16 v[34:49], v[62:65], v[66:69], v[34:49]
	ds_read2_b64 v[62:65], v114 offset0:28 offset1:30
	s_waitcnt lgkmcnt(1)
	v_mfma_f32_32x32x16_f16 v[18:33], v[58:61], v[70:73], v[18:33]
	s_waitcnt lgkmcnt(0)
	v_mfma_f32_32x32x16_f16 v[34:49], v[62:65], v[70:73], v[34:49]
	ds_read2_b64 v[58:61], v113 offset0:32 offset1:34
	ds_read2_b64 v[62:65], v114 offset0:32 offset1:34
	s_nop 1
	s_waitcnt lgkmcnt(1)
	v_mfma_f32_32x32x16_f16 v[18:33], v[58:61], v[50:53], v[18:33]
	ds_read2_b64 v[58:61], v113 offset0:36 offset1:38
	s_waitcnt lgkmcnt(1)
	v_mfma_f32_32x32x16_f16 v[34:49], v[62:65], v[50:53], v[34:49]
	ds_read2_b64 v[62:65], v114 offset0:36 offset1:38
	s_waitcnt lgkmcnt(1)
	v_mfma_f32_32x32x16_f16 v[18:33], v[58:61], v[54:57], v[18:33]
	s_waitcnt lgkmcnt(0)
	v_mfma_f32_32x32x16_f16 v[34:49], v[62:65], v[54:57], v[34:49]
	ds_read2_b64 v[58:61], v113 offset0:40 offset1:42
	ds_read2_b64 v[62:65], v114 offset0:40 offset1:42
	s_nop 1
	s_waitcnt lgkmcnt(1)
	v_mfma_f32_32x32x16_f16 v[18:33], v[58:61], v[116:119], v[18:33]
	ds_read2_b64 v[58:61], v113 offset0:44 offset1:46
	s_waitcnt lgkmcnt(1)
	v_mfma_f32_32x32x16_f16 v[34:49], v[62:65], v[116:119], v[34:49]
	ds_read2_b64 v[62:65], v114 offset0:44 offset1:46
	s_waitcnt lgkmcnt(1)
	v_mfma_f32_32x32x16_f16 v[18:33], v[58:61], v[124:127], v[18:33]
	s_waitcnt lgkmcnt(0)
	v_mfma_f32_32x32x16_f16 v[34:49], v[62:65], v[124:127], v[34:49]
	v_fma_f32 v120, v90, s16, -v106
	v_exp_f32_e32 v90, v120
	v_fma_f32 v121, v91, s16, -v106
	v_exp_f32_e32 v91, v121
	v_fma_f32 v122, v92, s16, -v106
	v_exp_f32_e32 v92, v122
	v_fma_f32 v123, v93, s16, -v106
	v_exp_f32_e32 v93, v123
	v_fma_f32 v120, v94, s16, -v106
	v_exp_f32_e32 v94, v120
	v_fma_f32 v121, v95, s16, -v106
	v_exp_f32_e32 v95, v121
	v_fma_f32 v122, v96, s16, -v106
	v_exp_f32_e32 v96, v122
	v_fma_f32 v123, v97, s16, -v106
	v_exp_f32_e32 v97, v123
	v_fma_f32 v120, v98, s16, -v106
	v_exp_f32_e32 v98, v120
	v_fma_f32 v121, v99, s16, -v106
	v_exp_f32_e32 v99, v121
	v_fma_f32 v122, v100, s16, -v106
	v_exp_f32_e32 v100, v122
	v_fma_f32 v123, v101, s16, -v106
	v_exp_f32_e32 v101, v123
	v_fma_f32 v120, v102, s16, -v106
	v_exp_f32_e32 v102, v120
	v_fma_f32 v121, v103, s16, -v106
	v_exp_f32_e32 v103, v121
	v_fma_f32 v122, v104, s16, -v106
	v_exp_f32_e32 v104, v122
	v_fma_f32 v123, v105, s16, -v106
	v_exp_f32_e32 v105, v123
	v_add_f32_e32 v107, v107, v90
	v_add_f32_e32 v107, v107, v91
	v_add_f32_e32 v107, v107, v92
	v_add_f32_e32 v107, v107, v93
	v_add_f32_e32 v107, v107, v94
	v_add_f32_e32 v107, v107, v95
	v_add_f32_e32 v107, v107, v96
	v_add_f32_e32 v107, v107, v97
	v_add_f32_e32 v107, v107, v98
	v_add_f32_e32 v107, v107, v99
	v_add_f32_e32 v107, v107, v100
	v_add_f32_e32 v107, v107, v101
	v_add_f32_e32 v107, v107, v102
	v_add_f32_e32 v107, v107, v103
	v_add_f32_e32 v107, v107, v104
	v_add_f32_e32 v107, v107, v105
	v_cvt_pk_f16_f32 v50, v90, v91
	v_cvt_pk_f16_f32 v51, v92, v93
	v_cvt_pk_f16_f32 v52, v94, v95
	v_cvt_pk_f16_f32 v53, v96, v97
	v_cvt_pk_f16_f32 v54, v98, v99
	v_cvt_pk_f16_f32 v55, v100, v101
	v_cvt_pk_f16_f32 v56, v102, v103
	v_cvt_pk_f16_f32 v57, v104, v105
	ds_read2_b64 v[58:61], v113 offset0:48 offset1:50
	ds_read2_b64 v[62:65], v114 offset0:48 offset1:50
	s_nop 1
	s_waitcnt lgkmcnt(1)
	v_mfma_f32_32x32x16_f16 v[18:33], v[58:61], v[50:53], v[18:33]
	ds_read2_b64 v[58:61], v113 offset0:52 offset1:54
	s_waitcnt lgkmcnt(1)
	v_mfma_f32_32x32x16_f16 v[34:49], v[62:65], v[50:53], v[34:49]
	ds_read2_b64 v[62:65], v114 offset0:52 offset1:54
	s_waitcnt lgkmcnt(1)
	v_mfma_f32_32x32x16_f16 v[18:33], v[58:61], v[54:57], v[18:33]
	s_waitcnt lgkmcnt(0)
	v_mfma_f32_32x32x16_f16 v[34:49], v[62:65], v[54:57], v[34:49]
	ds_read_b128 v[66:69], v112 offset:0
	ds_read_b128 v[70:73], v112 offset:32
	s_waitcnt lgkmcnt(1)
	v_mfma_f32_32x32x16_f16 v[90:105], v[66:69], v[74:77], 0
	ds_read_b128 v[66:69], v112 offset:64
	s_waitcnt lgkmcnt(1)
	v_mfma_f32_32x32x16_f16 v[90:105], v[70:73], v[78:81], v[90:105]
	ds_read_b128 v[70:73], v112 offset:96
	s_waitcnt lgkmcnt(1)
	v_mfma_f32_32x32x16_f16 v[90:105], v[66:69], v[82:85], v[90:105]
	s_waitcnt lgkmcnt(0)
	v_mfma_f32_32x32x16_f16 v[90:105], v[70:73], v[86:89], v[90:105]
	v_fma_f32 v120, v2, s16, -v106
	v_exp_f32_e32 v2, v120
	v_fma_f32 v121, v3, s16, -v106
	v_exp_f32_e32 v3, v121
	v_fma_f32 v122, v4, s16, -v106
	v_exp_f32_e32 v4, v122
	v_fma_f32 v123, v5, s16, -v106
	v_exp_f32_e32 v5, v123
	v_fma_f32 v120, v6, s16, -v106
	v_exp_f32_e32 v6, v120
	v_fma_f32 v121, v7, s16, -v106
	v_exp_f32_e32 v7, v121
	v_fma_f32 v122, v8, s16, -v106
	v_exp_f32_e32 v8, v122
	v_fma_f32 v123, v9, s16, -v106
	v_exp_f32_e32 v9, v123
	v_fma_f32 v120, v10, s16, -v106
	v_exp_f32_e32 v10, v120
	v_fma_f32 v121, v11, s16, -v106
	v_exp_f32_e32 v11, v121
	v_fma_f32 v122, v12, s16, -v106
	v_exp_f32_e32 v12, v122
	v_fma_f32 v123, v13, s16, -v106
	v_exp_f32_e32 v13, v123
	v_fma_f32 v120, v14, s16, -v106
	v_exp_f32_e32 v14, v120
	v_fma_f32 v121, v15, s16, -v106
	v_exp_f32_e32 v15, v121
	v_fma_f32 v122, v16, s16, -v106
	v_exp_f32_e32 v16, v122
	v_fma_f32 v123, v17, s16, -v106
	v_exp_f32_e32 v17, v123
	v_add_f32_e32 v107, v107, v2
	v_add_f32_e32 v107, v107, v3
	v_add_f32_e32 v107, v107, v4
	v_add_f32_e32 v107, v107, v5
	v_add_f32_e32 v107, v107, v6
	v_add_f32_e32 v107, v107, v7
	v_add_f32_e32 v107, v107, v8
	v_add_f32_e32 v107, v107, v9
	v_add_f32_e32 v107, v107, v10
	v_add_f32_e32 v107, v107, v11
	v_add_f32_e32 v107, v107, v12
	v_add_f32_e32 v107, v107, v13
	v_add_f32_e32 v107, v107, v14
	v_add_f32_e32 v107, v107, v15
	v_add_f32_e32 v107, v107, v16
	v_add_f32_e32 v107, v107, v17
	v_cvt_pk_f16_f32 v50, v2, v3
	v_cvt_pk_f16_f32 v51, v4, v5
	v_cvt_pk_f16_f32 v52, v6, v7
	v_cvt_pk_f16_f32 v53, v8, v9
	v_cvt_pk_f16_f32 v54, v10, v11
	v_cvt_pk_f16_f32 v55, v12, v13
	v_cvt_pk_f16_f32 v56, v14, v15
	v_cvt_pk_f16_f32 v57, v16, v17
	ds_read2_b64 v[58:61], v113 offset0:16 offset1:18
	ds_read2_b64 v[62:65], v114 offset0:16 offset1:18
	s_nop 1
	s_waitcnt lgkmcnt(1)
	v_mfma_f32_32x32x16_f16 v[18:33], v[58:61], v[50:53], v[18:33]
	ds_read2_b64 v[58:61], v113 offset0:20 offset1:22
	s_waitcnt lgkmcnt(1)
	v_mfma_f32_32x32x16_f16 v[34:49], v[62:65], v[50:53], v[34:49]
	ds_read2_b64 v[62:65], v114 offset0:20 offset1:22
	s_waitcnt lgkmcnt(1)
	v_mfma_f32_32x32x16_f16 v[18:33], v[58:61], v[54:57], v[18:33]
	s_waitcnt lgkmcnt(0)
	v_mfma_f32_32x32x16_f16 v[34:49], v[62:65], v[54:57], v[34:49]
	ds_read_b128 v[66:69], v112 offset:4608
	ds_read_b128 v[70:73], v112 offset:4640
	s_waitcnt lgkmcnt(1)
	v_mfma_f32_32x32x16_f16 v[2:17], v[66:69], v[74:77], 0
	ds_read_b128 v[66:69], v112 offset:4672
	s_waitcnt lgkmcnt(1)
	v_mfma_f32_32x32x16_f16 v[2:17], v[70:73], v[78:81], v[2:17]
	ds_read_b128 v[70:73], v112 offset:4704
	s_waitcnt lgkmcnt(1)
	v_mfma_f32_32x32x16_f16 v[2:17], v[66:69], v[82:85], v[2:17]
	s_waitcnt lgkmcnt(0)
	v_mfma_f32_32x32x16_f16 v[2:17], v[70:73], v[86:89], v[2:17]
	v_fma_f32 v120, v90, s16, -v106
	v_exp_f32_e32 v90, v120
	v_fma_f32 v121, v91, s16, -v106
	v_exp_f32_e32 v91, v121
	v_fma_f32 v122, v92, s16, -v106
	v_exp_f32_e32 v92, v122
	v_fma_f32 v123, v93, s16, -v106
	v_exp_f32_e32 v93, v123
	v_fma_f32 v120, v94, s16, -v106
	v_exp_f32_e32 v94, v120
	v_fma_f32 v121, v95, s16, -v106
	v_exp_f32_e32 v95, v121
	v_fma_f32 v122, v96, s16, -v106
	v_exp_f32_e32 v96, v122
	v_fma_f32 v123, v97, s16, -v106
	v_exp_f32_e32 v97, v123
	v_fma_f32 v120, v98, s16, -v106
	v_exp_f32_e32 v98, v120
	v_fma_f32 v121, v99, s16, -v106
	v_exp_f32_e32 v99, v121
	v_fma_f32 v122, v100, s16, -v106
	v_exp_f32_e32 v100, v122
	v_fma_f32 v123, v101, s16, -v106
	v_exp_f32_e32 v101, v123
	v_fma_f32 v120, v102, s16, -v106
	v_exp_f32_e32 v102, v120
	v_fma_f32 v121, v103, s16, -v106
	v_exp_f32_e32 v103, v121
	v_fma_f32 v122, v104, s16, -v106
	v_exp_f32_e32 v104, v122
	v_fma_f32 v123, v105, s16, -v106
	v_exp_f32_e32 v105, v123
	v_add_f32_e32 v107, v107, v90
	v_add_f32_e32 v107, v107, v91
	v_add_f32_e32 v107, v107, v92
	v_add_f32_e32 v107, v107, v93
	v_add_f32_e32 v107, v107, v94
	v_add_f32_e32 v107, v107, v95
	v_add_f32_e32 v107, v107, v96
	v_add_f32_e32 v107, v107, v97
	v_add_f32_e32 v107, v107, v98
	v_add_f32_e32 v107, v107, v99
	v_add_f32_e32 v107, v107, v100
	v_add_f32_e32 v107, v107, v101
	v_add_f32_e32 v107, v107, v102
	v_add_f32_e32 v107, v107, v103
	v_add_f32_e32 v107, v107, v104
	v_add_f32_e32 v107, v107, v105
	v_cvt_pk_f16_f32 v50, v90, v91
	v_cvt_pk_f16_f32 v51, v92, v93
	v_cvt_pk_f16_f32 v52, v94, v95
	v_cvt_pk_f16_f32 v53, v96, v97
	v_cvt_pk_f16_f32 v54, v98, v99
	v_cvt_pk_f16_f32 v55, v100, v101
	v_cvt_pk_f16_f32 v56, v102, v103
	v_cvt_pk_f16_f32 v57, v104, v105
	ds_read2_b64 v[58:61], v113 offset0:0 offset1:2
	ds_read2_b64 v[62:65], v114 offset0:0 offset1:2
	s_nop 1
	s_waitcnt lgkmcnt(1)
	v_mfma_f32_32x32x16_f16 v[18:33], v[58:61], v[50:53], v[18:33]
	ds_read2_b64 v[58:61], v113 offset0:4 offset1:6
	s_waitcnt lgkmcnt(1)
	v_mfma_f32_32x32x16_f16 v[34:49], v[62:65], v[50:53], v[34:49]
	ds_read2_b64 v[62:65], v114 offset0:4 offset1:6
	s_waitcnt lgkmcnt(1)
	v_mfma_f32_32x32x16_f16 v[18:33], v[58:61], v[54:57], v[18:33]
	s_waitcnt lgkmcnt(0)
	v_mfma_f32_32x32x16_f16 v[34:49], v[62:65], v[54:57], v[34:49]
	s_nop 15
	s_nop 1
	v_fma_f32 v120, v2, s16, -v106
	v_exp_f32_e32 v2, v120
	v_fma_f32 v121, v3, s16, -v106
	v_exp_f32_e32 v3, v121
	v_fma_f32 v122, v4, s16, -v106
	v_exp_f32_e32 v4, v122
	v_fma_f32 v123, v5, s16, -v106
	v_exp_f32_e32 v5, v123
	v_fma_f32 v120, v6, s16, -v106
	v_exp_f32_e32 v6, v120
	v_fma_f32 v121, v7, s16, -v106
	v_exp_f32_e32 v7, v121
	v_fma_f32 v122, v8, s16, -v106
	v_exp_f32_e32 v8, v122
	v_fma_f32 v123, v9, s16, -v106
	v_exp_f32_e32 v9, v123
	v_fma_f32 v120, v10, s16, -v106
	v_exp_f32_e32 v10, v120
	v_fma_f32 v121, v11, s16, -v106
	v_exp_f32_e32 v11, v121
	v_fma_f32 v122, v12, s16, -v106
	v_exp_f32_e32 v12, v122
	v_fma_f32 v123, v13, s16, -v106
	v_exp_f32_e32 v13, v123
	v_fma_f32 v120, v14, s16, -v106
	v_exp_f32_e32 v14, v120
	v_fma_f32 v121, v15, s16, -v106
	v_exp_f32_e32 v15, v121
	v_fma_f32 v122, v16, s16, -v106
	v_exp_f32_e32 v16, v122
	v_fma_f32 v123, v17, s16, -v106
	v_exp_f32_e32 v17, v123
	v_add_f32_e32 v107, v107, v2
	v_add_f32_e32 v107, v107, v3
	v_add_f32_e32 v107, v107, v4
	v_add_f32_e32 v107, v107, v5
	v_add_f32_e32 v107, v107, v6
	v_add_f32_e32 v107, v107, v7
	v_add_f32_e32 v107, v107, v8
	v_add_f32_e32 v107, v107, v9
	v_add_f32_e32 v107, v107, v10
	v_add_f32_e32 v107, v107, v11
	v_add_f32_e32 v107, v107, v12
	v_add_f32_e32 v107, v107, v13
	v_add_f32_e32 v107, v107, v14
	v_add_f32_e32 v107, v107, v15
	v_add_f32_e32 v107, v107, v16
	v_add_f32_e32 v107, v107, v17
	v_cvt_pk_f16_f32 v50, v2, v3
	v_cvt_pk_f16_f32 v51, v4, v5
	v_cvt_pk_f16_f32 v52, v6, v7
	v_cvt_pk_f16_f32 v53, v8, v9
	v_cvt_pk_f16_f32 v54, v10, v11
	v_cvt_pk_f16_f32 v55, v12, v13
	v_cvt_pk_f16_f32 v56, v14, v15
	v_cvt_pk_f16_f32 v57, v16, v17
	ds_read2_b64 v[58:61], v113 offset0:8 offset1:10
	ds_read2_b64 v[62:65], v114 offset0:8 offset1:10
	s_nop 1
	s_waitcnt lgkmcnt(1)
	v_mfma_f32_32x32x16_f16 v[18:33], v[58:61], v[50:53], v[18:33]
	ds_read2_b64 v[58:61], v113 offset0:12 offset1:14
	s_waitcnt lgkmcnt(1)
	v_mfma_f32_32x32x16_f16 v[34:49], v[62:65], v[50:53], v[34:49]
	ds_read2_b64 v[62:65], v114 offset0:12 offset1:14
	s_waitcnt lgkmcnt(1)
	v_mfma_f32_32x32x16_f16 v[18:33], v[58:61], v[54:57], v[18:33]
	s_waitcnt lgkmcnt(0)
	v_mfma_f32_32x32x16_f16 v[34:49], v[62:65], v[54:57], v[34:49]
	v_mov_b32_e32 v120, v107
	v_mov_b32_e32 v121, v107
	s_nop 1
	v_permlane32_swap_b32_e32 v120, v121
	s_nop 1
	v_add_f32_e32 v107, v120, v121
	v_log_f32_e32 v122, v107
	v_rcp_f32_e32 v123, v107
	s_nop 0
	v_add_f32_e32 v122, v122, v106
	v_fma_f32 v124, -v107, v123, 2.0
	v_mul_f32_e32 v123, v123, v124
	v_lshlrev_b32_e32 v125, 2, v109
	s_mov_b64 s[18:19], exec
	s_and_b64 exec, exec, s[14:15]
	ds_write_b32 v125, v122 offset:61440
	s_mov_b64 exec, s[18:19]
	s_mul_i32 s20, s2, 0x493
	s_lshr_b32 s20, s20, 16
	s_mul_i32 s21, s20, 56
	s_sub_u32 s21, s2, s21
	s_mul_i32 s22, s21, 0x2493
	s_lshr_b32 s22, s22, 16
	s_mul_i32 s23, s22, 7
	s_sub_u32 s23, s21, s23
	s_mul_i32 s24, s23, 0xc5
	s_lshl_b32 s24, s24, 13
	s_lshl_b32 s25, s22, 10
	s_add_u32 s24, s24, s25
	s_lshl_b32 s25, s20, 7
	s_add_u32 s24, s24, s25
	v_lshlrev_b32_e32 v125, 13, v110
	v_add3_u32 v125, v125, s24, v111
	s_nop 15
	s_waitcnt lgkmcnt(0)
	v_mul_f32_e32 v18, v18, v123
	v_mul_f32_e32 v19, v19, v123
	v_mul_f32_e32 v20, v20, v123
	v_mul_f32_e32 v21, v21, v123
	v_mul_f32_e32 v22, v22, v123
	v_mul_f32_e32 v23, v23, v123
	v_mul_f32_e32 v24, v24, v123
	v_mul_f32_e32 v25, v25, v123
	v_cvt_pk_f16_f32 v50, v18, v19
	v_cvt_pk_f16_f32 v51, v20, v21
	v_cvt_pk_f16_f32 v52, v22, v23
	v_cvt_pk_f16_f32 v53, v24, v25
	s_nop 1
	v_permlane32_swap_b32_e32 v50, v52
	v_permlane32_swap_b32_e32 v51, v53
	s_nop 1
	s_and_b64 exec, exec, s[12:13]
	global_store_dwordx4 v125, v[50:53], s[8:9] offset:0
	s_mov_b64 exec, s[18:19]
	s_nop 1
	v_mul_f32_e32 v26, v26, v123
	v_mul_f32_e32 v27, v27, v123
	v_mul_f32_e32 v28, v28, v123
	v_mul_f32_e32 v29, v29, v123
	v_mul_f32_e32 v30, v30, v123
	v_mul_f32_e32 v31, v31, v123
	v_mul_f32_e32 v32, v32, v123
	v_mul_f32_e32 v33, v33, v123
	v_cvt_pk_f16_f32 v54, v26, v27
	v_cvt_pk_f16_f32 v55, v28, v29
	v_cvt_pk_f16_f32 v56, v30, v31
	v_cvt_pk_f16_f32 v57, v32, v33
	s_nop 1
	v_permlane32_swap_b32_e32 v54, v56
	v_permlane32_swap_b32_e32 v55, v57
	s_nop 1
	s_and_b64 exec, exec, s[12:13]
	global_store_dwordx4 v125, v[54:57], s[8:9] offset:32
	s_mov_b64 exec, s[18:19]
	s_nop 1
	v_mul_f32_e32 v34, v34, v123
	v_mul_f32_e32 v35, v35, v123
	v_mul_f32_e32 v36, v36, v123
	v_mul_f32_e32 v37, v37, v123
	v_mul_f32_e32 v38, v38, v123
	v_mul_f32_e32 v39, v39, v123
	v_mul_f32_e32 v40, v40, v123
	v_mul_f32_e32 v41, v41, v123
	v_cvt_pk_f16_f32 v50, v34, v35
	v_cvt_pk_f16_f32 v51, v36, v37
	v_cvt_pk_f16_f32 v52, v38, v39
	v_cvt_pk_f16_f32 v53, v40, v41
	s_nop 1
	v_permlane32_swap_b32_e32 v50, v52
	v_permlane32_swap_b32_e32 v51, v53
	s_nop 1
	s_and_b64 exec, exec, s[12:13]
	global_store_dwordx4 v125, v[50:53], s[8:9] offset:64
	s_mov_b64 exec, s[18:19]
	s_nop 1
	v_mul_f32_e32 v42, v42, v123
	v_mul_f32_e32 v43, v43, v123
	v_mul_f32_e32 v44, v44, v123
	v_mul_f32_e32 v45, v45, v123
	v_mul_f32_e32 v46, v46, v123
	v_mul_f32_e32 v47, v47, v123
	v_mul_f32_e32 v48, v48, v123
	v_mul_f32_e32 v49, v49, v123
	v_cvt_pk_f16_f32 v54, v42, v43
	v_cvt_pk_f16_f32 v55, v44, v45
	v_cvt_pk_f16_f32 v56, v46, v47
	v_cvt_pk_f16_f32 v57, v48, v49
	s_nop 1
	v_permlane32_swap_b32_e32 v54, v56
	v_permlane32_swap_b32_e32 v55, v57
	s_nop 1
	s_and_b64 exec, exec, s[12:13]
	global_store_dwordx4 v125, v[54:57], s[8:9] offset:96
	s_mov_b64 exec, s[18:19]
	s_nop 1
	s_waitcnt lgkmcnt(0)
	s_barrier
	v_lshl_add_u32 v120, v115, 2, v111
	ds_read_b128 v[90:93], v120 offset:61440
	ds_read_b128 v[94:97], v120 offset:61472
	ds_read_b128 v[98:101], v120 offset:61504
	ds_read_b128 v[102:105], v120 offset:61536
	v_lshl_or_b32 v121, v1, 2, v115
	v_mul_u32_u24_e32 v121, 0xc5, v121
	v_add_lshl_u32 v116, v121, v108, 2
	v_add_u32_e32 v117, 0x18a0, v116
	v_add_u32_e32 v118, 0x3140, v116
	v_add_u32_e32 v119, 0x49e0, v116
	s_mul_hi_u32 s21, s2, 0x25e64
	s_mul_i32 s20, s2, 0x25e64
	s_add_u32 s10, s10, s20
	s_addc_u32 s11, s11, s21
	v_cmp_gt_u32_e64 s[22:23], 5, v108
	s_nop 0
	v_readfirstlane_b32 s26, v115
	s_cmp_eq_u32 s26, 0xc0
	s_cbranch_scc1 .Lsp_wave6
	ds_read_b128 v[66:69], v112 offset:0
	ds_read_b128 v[70:73], v112 offset:32
	s_waitcnt lgkmcnt(1)
	v_mfma_f32_32x32x16_f16 v[2:17], v[74:77], v[66:69], 0
	ds_read_b128 v[66:69], v112 offset:64
	s_waitcnt lgkmcnt(1)
	v_mfma_f32_32x32x16_f16 v[2:17], v[78:81], v[70:73], v[2:17]
	ds_read_b128 v[70:73], v112 offset:96
	s_waitcnt lgkmcnt(1)
	v_mfma_f32_32x32x16_f16 v[2:17], v[82:85], v[66:69], v[2:17]
	s_waitcnt lgkmcnt(0)
	v_mfma_f32_32x32x16_f16 v[2:17], v[86:89], v[70:73], v[2:17]
	s_waitcnt lgkmcnt(0)
	ds_read_b128 v[66:69], v112 offset:4608
	ds_read_b128 v[70:73], v112 offset:4640
	s_waitcnt lgkmcnt(1)
	v_mfma_f32_32x32x16_f16 v[18:33], v[74:77], v[66:69], 0
	ds_read_b128 v[66:69], v112 offset:4672
	s_waitcnt lgkmcnt(1)
	v_mfma_f32_32x32x16_f16 v[18:33], v[78:81], v[70:73], v[18:33]
	ds_read_b128 v[70:73], v112 offset:4704
	s_waitcnt lgkmcnt(1)
	v_mfma_f32_32x32x16_f16 v[18:33], v[82:85], v[66:69], v[18:33]
	s_waitcnt lgkmcnt(0)
	v_mfma_f32_32x32x16_f16 v[18:33], v[86:89], v[70:73], v[18:33]
	v_fma_f32 v120, v2, s16, -v90
	v_exp_f32_e32 v2, v120
	v_fma_f32 v121, v3, s16, -v91
	v_exp_f32_e32 v3, v121
	v_fma_f32 v122, v4, s16, -v92
	v_exp_f32_e32 v4, v122
	v_fma_f32 v123, v5, s16, -v93
	v_exp_f32_e32 v5, v123
	v_fma_f32 v120, v6, s16, -v94
	v_exp_f32_e32 v6, v120
	v_fma_f32 v121, v7, s16, -v95
	v_exp_f32_e32 v7, v121
	v_fma_f32 v122, v8, s16, -v96
	v_exp_f32_e32 v8, v122
	v_fma_f32 v123, v9, s16, -v97
	v_exp_f32_e32 v9, v123
	v_fma_f32 v120, v10, s16, -v98
	v_exp_f32_e32 v10, v120
	v_fma_f32 v121, v11, s16, -v99
	v_exp_f32_e32 v11, v121
	v_fma_f32 v122, v12, s16, -v100
	v_exp_f32_e32 v12, v122
	v_fma_f32 v123, v13, s16, -v101
	v_exp_f32_e32 v13, v123
	v_fma_f32 v120, v14, s16, -v102
	v_exp_f32_e32 v14, v120
	v_fma_f32 v121, v15, s16, -v103
	v_exp_f32_e32 v15, v121
	v_fma_f32 v122, v16, s16, -v104
	v_exp_f32_e32 v16, v122
	v_fma_f32 v123, v17, s16, -v105
	v_exp_f32_e32 v17, v123
	global_store_dword v116, v2, s[10:11] offset:0
	global_store_dword v116, v3, s[10:11] offset:788
	global_store_dword v116, v4, s[10:11] offset:1576
	global_store_dword v116, v5, s[10:11] offset:2364
	global_store_dword v117, v6, s[10:11] offset:0
	global_store_dword v117, v7, s[10:11] offset:788
	global_store_dword v117, v8, s[10:11] offset:1576
	global_store_dword v117, v9, s[10:11] offset:2364
	global_store_dword v118, v10, s[10:11] offset:0
	global_store_dword v118, v11, s[10:11] offset:788
	global_store_dword v118, v12, s[10:11] offset:1576
	global_store_dword v118, v13, s[10:11] offset:2364
	global_store_dword v119, v14, s[10:11] offset:0
	global_store_dword v119, v15, s[10:11] offset:788
	global_store_dword v119, v16, s[10:11] offset:1576
	global_store_dword v119, v17, s[10:11] offset:2364
	ds_read_b128 v[66:69], v112 offset:9216
	ds_read_b128 v[70:73], v112 offset:9248
	s_waitcnt lgkmcnt(1)
	v_mfma_f32_32x32x16_f16 v[2:17], v[74:77], v[66:69], 0
	ds_read_b128 v[66:69], v112 offset:9280
	s_waitcnt lgkmcnt(1)
	v_mfma_f32_32x32x16_f16 v[2:17], v[78:81], v[70:73], v[2:17]
	ds_read_b128 v[70:73], v112 offset:9312
	s_waitcnt lgkmcnt(1)
	v_mfma_f32_32x32x16_f16 v[2:17], v[82:85], v[66:69], v[2:17]
	s_waitcnt lgkmcnt(0)
	v_mfma_f32_32x32x16_f16 v[2:17], v[86:89], v[70:73], v[2:17]
	v_fma_f32 v120, v18, s16, -v90
	v_exp_f32_e32 v18, v120
	v_fma_f32 v121, v19, s16, -v91
	v_exp_f32_e32 v19, v121
	v_fma_f32 v122, v20, s16, -v92
	v_exp_f32_e32 v20, v122
	v_fma_f32 v123, v21, s16, -v93
	v_exp_f32_e32 v21, v123
	v_fma_f32 v120, v22, s16, -v94
	v_exp_f32_e32 v22, v120
	v_fma_f32 v121, v23, s16, -v95
	v_exp_f32_e32 v23, v121
	v_fma_f32 v122, v24, s16, -v96
	v_exp_f32_e32 v24, v122
	v_fma_f32 v123, v25, s16, -v97
	v_exp_f32_e32 v25, v123
	v_fma_f32 v120, v26, s16, -v98
	v_exp_f32_e32 v26, v120
	v_fma_f32 v121, v27, s16, -v99
	v_exp_f32_e32 v27, v121
	v_fma_f32 v122, v28, s16, -v100
	v_exp_f32_e32 v28, v122
	v_fma_f32 v123, v29, s16, -v101
	v_exp_f32_e32 v29, v123
	v_fma_f32 v120, v30, s16, -v102
	v_exp_f32_e32 v30, v120
	v_fma_f32 v121, v31, s16, -v103
	v_exp_f32_e32 v31, v121
	v_fma_f32 v122, v32, s16, -v104
	v_exp_f32_e32 v32, v122
	v_fma_f32 v123, v33, s16, -v105
	v_exp_f32_e32 v33, v123
	global_store_dword v116, v18, s[10:11] offset:128
	global_store_dword v116, v19, s[10:11] offset:916
	global_store_dword v116, v20, s[10:11] offset:1704
	global_store_dword v116, v21, s[10:11] offset:2492
	global_store_dword v117, v22, s[10:11] offset:128
	global_store_dword v117, v23, s[10:11] offset:916
	global_store_dword v117, v24, s[10:11] offset:1704
	global_store_dword v117, v25, s[10:11] offset:2492
	global_store_dword v118, v26, s[10:11] offset:128
	global_store_dword v118, v27, s[10:11] offset:916
	global_store_dword v118, v28, s[10:11] offset:1704
	global_store_dword v118, v29, s[10:11] offset:2492
	global_store_dword v119, v30, s[10:11] offset:128
	global_store_dword v119, v31, s[10:11] offset:916
	global_store_dword v119, v32, s[10:11] offset:1704
	global_store_dword v119, v33, s[10:11] offset:2492
	ds_read_b128 v[66:69], v112 offset:13824
	ds_read_b128 v[70:73], v112 offset:13856
	s_waitcnt lgkmcnt(1)
	v_mfma_f32_32x32x16_f16 v[18:33], v[74:77], v[66:69], 0
	ds_read_b128 v[66:69], v112 offset:13888
	s_waitcnt lgkmcnt(1)
	v_mfma_f32_32x32x16_f16 v[18:33], v[78:81], v[70:73], v[18:33]
	ds_read_b128 v[70:73], v112 offset:13920
	s_waitcnt lgkmcnt(1)
	v_mfma_f32_32x32x16_f16 v[18:33], v[82:85], v[66:69], v[18:33]
	s_waitcnt lgkmcnt(0)
	v_mfma_f32_32x32x16_f16 v[18:33], v[86:89], v[70:73], v[18:33]
	v_fma_f32 v120, v2, s16, -v90
	v_exp_f32_e32 v2, v120
	v_fma_f32 v121, v3, s16, -v91
	v_exp_f32_e32 v3, v121
	v_fma_f32 v122, v4, s16, -v92
	v_exp_f32_e32 v4, v122
	v_fma_f32 v123, v5, s16, -v93
	v_exp_f32_e32 v5, v123
	v_fma_f32 v120, v6, s16, -v94
	v_exp_f32_e32 v6, v120
	v_fma_f32 v121, v7, s16, -v95
	v_exp_f32_e32 v7, v121
	v_fma_f32 v122, v8, s16, -v96
	v_exp_f32_e32 v8, v122
	v_fma_f32 v123, v9, s16, -v97
	v_exp_f32_e32 v9, v123
	v_fma_f32 v120, v10, s16, -v98
	v_exp_f32_e32 v10, v120
	v_fma_f32 v121, v11, s16, -v99
	v_exp_f32_e32 v11, v121
	v_fma_f32 v122, v12, s16, -v100
	v_exp_f32_e32 v12, v122
	v_fma_f32 v123, v13, s16, -v101
	v_exp_f32_e32 v13, v123
	v_fma_f32 v120, v14, s16, -v102
	v_exp_f32_e32 v14, v120
	v_fma_f32 v121, v15, s16, -v103
	v_exp_f32_e32 v15, v121
	v_fma_f32 v122, v16, s16, -v104
	v_exp_f32_e32 v16, v122
	v_fma_f32 v123, v17, s16, -v105
	v_exp_f32_e32 v17, v123
	global_store_dword v116, v2, s[10:11] offset:256
	global_store_dword v116, v3, s[10:11] offset:1044
	global_store_dword v116, v4, s[10:11] offset:1832
	global_store_dword v116, v5, s[10:11] offset:2620
	global_store_dword v117, v6, s[10:11] offset:256
	global_store_dword v117, v7, s[10:11] offset:1044
	global_store_dword v117, v8, s[10:11] offset:1832
	global_store_dword v117, v9, s[10:11] offset:2620
	global_store_dword v118, v10, s[10:11] offset:256
	global_store_dword v118, v11, s[10:11] offset:1044
	global_store_dword v118, v12, s[10:11] offset:1832
	global_store_dword v118, v13, s[10:11] offset:2620
	global_store_dword v119, v14, s[10:11] offset:256
	global_store_dword v119, v15, s[10:11] offset:1044
	global_store_dword v119, v16, s[10:11] offset:1832
	global_store_dword v119, v17, s[10:11] offset:2620
	ds_read_b128 v[66:69], v112 offset:18432
	ds_read_b128 v[70:73], v112 offset:18464
	s_waitcnt lgkmcnt(1)
	v_mfma_f32_32x32x16_f16 v[2:17], v[74:77], v[66:69], 0
	ds_read_b128 v[66:69], v112 offset:18496
	s_waitcnt lgkmcnt(1)
	v_mfma_f32_32x32x16_f16 v[2:17], v[78:81], v[70:73], v[2:17]
	ds_read_b128 v[70:73], v112 offset:18528
	s_waitcnt lgkmcnt(1)
	v_mfma_f32_32x32x16_f16 v[2:17], v[82:85], v[66:69], v[2:17]
	s_waitcnt lgkmcnt(0)
	v_mfma_f32_32x32x16_f16 v[2:17], v[86:89], v[70:73], v[2:17]
	v_fma_f32 v120, v18, s16, -v90
	v_exp_f32_e32 v18, v120
	v_fma_f32 v121, v19, s16, -v91
	v_exp_f32_e32 v19, v121
	v_fma_f32 v122, v20, s16, -v92
	v_exp_f32_e32 v20, v122
	v_fma_f32 v123, v21, s16, -v93
	v_exp_f32_e32 v21, v123
	v_fma_f32 v120, v22, s16, -v94
	v_exp_f32_e32 v22, v120
	v_fma_f32 v121, v23, s16, -v95
	v_exp_f32_e32 v23, v121
	v_fma_f32 v122, v24, s16, -v96
	v_exp_f32_e32 v24, v122
	v_fma_f32 v123, v25, s16, -v97
	v_exp_f32_e32 v25, v123
	v_fma_f32 v120, v26, s16, -v98
	v_exp_f32_e32 v26, v120
	v_fma_f32 v121, v27, s16, -v99
	v_exp_f32_e32 v27, v121
	v_fma_f32 v122, v28, s16, -v100
	v_exp_f32_e32 v28, v122
	v_fma_f32 v123, v29, s16, -v101
	v_exp_f32_e32 v29, v123
	v_fma_f32 v120, v30, s16, -v102
	v_exp_f32_e32 v30, v120
	v_fma_f32 v121, v31, s16, -v103
	v_exp_f32_e32 v31, v121
	v_fma_f32 v122, v32, s16, -v104
	v_exp_f32_e32 v32, v122
	v_fma_f32 v123, v33, s16, -v105
	v_exp_f32_e32 v33, v123
	global_store_dword v116, v18, s[10:11] offset:384
	global_store_dword v116, v19, s[10:11] offset:1172
	global_store_dword v116, v20, s[10:11] offset:1960
	global_store_dword v116, v21, s[10:11] offset:2748
	global_store_dword v117, v22, s[10:11] offset:384
	global_store_dword v117, v23, s[10:11] offset:1172
	global_store_dword v117, v24, s[10:11] offset:1960
	global_store_dword v117, v25, s[10:11] offset:2748
	global_store_dword v118, v26, s[10:11] offset:384
	global_store_dword v118, v27, s[10:11] offset:1172
	global_store_dword v118, v28, s[10:11] offset:1960
	global_store_dword v118, v29, s[10:11] offset:2748
	global_store_dword v119, v30, s[10:11] offset:384
	global_store_dword v119, v31, s[10:11] offset:1172
	global_store_dword v119, v32, s[10:11] offset:1960
	global_store_dword v119, v33, s[10:11] offset:2748
	ds_read_b128 v[66:69], v112 offset:23040
	ds_read_b128 v[70:73], v112 offset:23072
	s_waitcnt lgkmcnt(1)
	v_mfma_f32_32x32x16_f16 v[18:33], v[74:77], v[66:69], 0
	ds_read_b128 v[66:69], v112 offset:23104
	s_waitcnt lgkmcnt(1)
	v_mfma_f32_32x32x16_f16 v[18:33], v[78:81], v[70:73], v[18:33]
	ds_read_b128 v[70:73], v112 offset:23136
	s_waitcnt lgkmcnt(1)
	v_mfma_f32_32x32x16_f16 v[18:33], v[82:85], v[66:69], v[18:33]
	s_waitcnt lgkmcnt(0)
	v_mfma_f32_32x32x16_f16 v[18:33], v[86:89], v[70:73], v[18:33]
	v_fma_f32 v120, v2, s16, -v90
	v_exp_f32_e32 v2, v120
	v_fma_f32 v121, v3, s16, -v91
	v_exp_f32_e32 v3, v121
	v_fma_f32 v122, v4, s16, -v92
	v_exp_f32_e32 v4, v122
	v_fma_f32 v123, v5, s16, -v93
	v_exp_f32_e32 v5, v123
	v_fma_f32 v120, v6, s16, -v94
	v_exp_f32_e32 v6, v120
	v_fma_f32 v121, v7, s16, -v95
	v_exp_f32_e32 v7, v121
	v_fma_f32 v122, v8, s16, -v96
	v_exp_f32_e32 v8, v122
	v_fma_f32 v123, v9, s16, -v97
	v_exp_f32_e32 v9, v123
	v_fma_f32 v120, v10, s16, -v98
	v_exp_f32_e32 v10, v120
	v_fma_f32 v121, v11, s16, -v99
	v_exp_f32_e32 v11, v121
	v_fma_f32 v122, v12, s16, -v100
	v_exp_f32_e32 v12, v122
	v_fma_f32 v123, v13, s16, -v101
	v_exp_f32_e32 v13, v123
	v_fma_f32 v120, v14, s16, -v102
	v_exp_f32_e32 v14, v120
	v_fma_f32 v121, v15, s16, -v103
	v_exp_f32_e32 v15, v121
	v_fma_f32 v122, v16, s16, -v104
	v_exp_f32_e32 v16, v122
	v_fma_f32 v123, v17, s16, -v105
	v_exp_f32_e32 v17, v123
	global_store_dword v116, v2, s[10:11] offset:512
	global_store_dword v116, v3, s[10:11] offset:1300
	global_store_dword v116, v4, s[10:11] offset:2088
	global_store_dword v116, v5, s[10:11] offset:2876
	global_store_dword v117, v6, s[10:11] offset:512
	global_store_dword v117, v7, s[10:11] offset:1300
	global_store_dword v117, v8, s[10:11] offset:2088
	global_store_dword v117, v9, s[10:11] offset:2876
	global_store_dword v118, v10, s[10:11] offset:512
	global_store_dword v118, v11, s[10:11] offset:1300
	global_store_dword v118, v12, s[10:11] offset:2088
	global_store_dword v118, v13, s[10:11] offset:2876
	global_store_dword v119, v14, s[10:11] offset:512
	global_store_dword v119, v15, s[10:11] offset:1300
	global_store_dword v119, v16, s[10:11] offset:2088
	global_store_dword v119, v17, s[10:11] offset:2876
	ds_read_b128 v[66:69], v112 offset:27648
	ds_read_b128 v[70:73], v112 offset:27680
	s_waitcnt lgkmcnt(1)
	v_mfma_f32_32x32x16_f16 v[2:17], v[74:77], v[66:69], 0
	ds_read_b128 v[66:69], v112 offset:27712
	s_waitcnt lgkmcnt(1)
	v_mfma_f32_32x32x16_f16 v[2:17], v[78:81], v[70:73], v[2:17]
	ds_read_b128 v[70:73], v112 offset:27744
	s_waitcnt lgkmcnt(1)
	v_mfma_f32_32x32x16_f16 v[2:17], v[82:85], v[66:69], v[2:17]
	s_waitcnt lgkmcnt(0)
	v_mfma_f32_32x32x16_f16 v[2:17], v[86:89], v[70:73], v[2:17]
	v_fma_f32 v120, v18, s16, -v90
	v_exp_f32_e32 v18, v120
	v_fma_f32 v121, v19, s16, -v91
	v_exp_f32_e32 v19, v121
	v_fma_f32 v122, v20, s16, -v92
	v_exp_f32_e32 v20, v122
	v_fma_f32 v123, v21, s16, -v93
	v_exp_f32_e32 v21, v123
	v_fma_f32 v120, v22, s16, -v94
	v_exp_f32_e32 v22, v120
	v_fma_f32 v121, v23, s16, -v95
	v_exp_f32_e32 v23, v121
	v_fma_f32 v122, v24, s16, -v96
	v_exp_f32_e32 v24, v122
	v_fma_f32 v123, v25, s16, -v97
	v_exp_f32_e32 v25, v123
	v_fma_f32 v120, v26, s16, -v98
	v_exp_f32_e32 v26, v120
	v_fma_f32 v121, v27, s16, -v99
	v_exp_f32_e32 v27, v121
	v_fma_f32 v122, v28, s16, -v100
	v_exp_f32_e32 v28, v122
	v_fma_f32 v123, v29, s16, -v101
	v_exp_f32_e32 v29, v123
	v_fma_f32 v120, v30, s16, -v102
	v_exp_f32_e32 v30, v120
	v_fma_f32 v121, v31, s16, -v103
	v_exp_f32_e32 v31, v121
	v_fma_f32 v122, v32, s16, -v104
	v_exp_f32_e32 v32, v122
	v_fma_f32 v123, v33, s16, -v105
	v_exp_f32_e32 v33, v123
	global_store_dword v116, v18, s[10:11] offset:640
	global_store_dword v116, v19, s[10:11] offset:1428
	global_store_dword v116, v20, s[10:11] offset:2216
	global_store_dword v116, v21, s[10:11] offset:3004
	global_store_dword v117, v22, s[10:11] offset:640
	global_store_dword v117, v23, s[10:11] offset:1428
	global_store_dword v117, v24, s[10:11] offset:2216
	global_store_dword v117, v25, s[10:11] offset:3004
	global_store_dword v118, v26, s[10:11] offset:640
	global_store_dword v118, v27, s[10:11] offset:1428
	global_store_dword v118, v28, s[10:11] offset:2216
	global_store_dword v118, v29, s[10:11] offset:3004
	global_store_dword v119, v30, s[10:11] offset:640
	global_store_dword v119, v31, s[10:11] offset:1428
	global_store_dword v119, v32, s[10:11] offset:2216
	global_store_dword v119, v33, s[10:11] offset:3004
	s_nop 15
	s_nop 1
	v_fma_f32 v120, v2, s16, -v90
	v_exp_f32_e32 v2, v120
	v_fma_f32 v121, v3, s16, -v91
	v_exp_f32_e32 v3, v121
	v_fma_f32 v122, v4, s16, -v92
	v_exp_f32_e32 v4, v122
	v_fma_f32 v123, v5, s16, -v93
	v_exp_f32_e32 v5, v123
	v_fma_f32 v120, v6, s16, -v94
	v_exp_f32_e32 v6, v120
	v_fma_f32 v121, v7, s16, -v95
	v_exp_f32_e32 v7, v121
	v_fma_f32 v122, v8, s16, -v96
	v_exp_f32_e32 v8, v122
	v_fma_f32 v123, v9, s16, -v97
	v_exp_f32_e32 v9, v123
	v_fma_f32 v120, v10, s16, -v98
	v_exp_f32_e32 v10, v120
	v_fma_f32 v121, v11, s16, -v99
	v_exp_f32_e32 v11, v121
	v_fma_f32 v122, v12, s16, -v100
	v_exp_f32_e32 v12, v122
	v_fma_f32 v123, v13, s16, -v101
	v_exp_f32_e32 v13, v123
	v_fma_f32 v120, v14, s16, -v102
	v_exp_f32_e32 v14, v120
	v_fma_f32 v121, v15, s16, -v103
	v_exp_f32_e32 v15, v121
	v_fma_f32 v122, v16, s16, -v104
	v_exp_f32_e32 v16, v122
	v_fma_f32 v123, v17, s16, -v105
	v_exp_f32_e32 v17, v123
	s_and_b64 exec, exec, s[22:23]
	global_store_dword v116, v2, s[10:11] offset:768
	global_store_dword v116, v3, s[10:11] offset:1556
	global_store_dword v116, v4, s[10:11] offset:2344
	global_store_dword v116, v5, s[10:11] offset:3132
	global_store_dword v117, v6, s[10:11] offset:768
	global_store_dword v117, v7, s[10:11] offset:1556
	global_store_dword v117, v8, s[10:11] offset:2344
	global_store_dword v117, v9, s[10:11] offset:3132
	global_store_dword v118, v10, s[10:11] offset:768
	global_store_dword v118, v11, s[10:11] offset:1556
	global_store_dword v118, v12, s[10:11] offset:2344
	global_store_dword v118, v13, s[10:11] offset:3132
	global_store_dword v119, v14, s[10:11] offset:768
	global_store_dword v119, v15, s[10:11] offset:1556
	global_store_dword v119, v16, s[10:11] offset:2344
	global_store_dword v119, v17, s[10:11] offset:3132
	s_mov_b64 exec, s[18:19]
	s_endpgm
